# v15
# baseline (speedup 1.0000x reference)
.Lnerf_enc_done:
	v_mov_b32_e32 v183, v131
	s_mov_b32 s50, 0x10000
	s_mov_b32 s52, 0
	v_or_b32_e32 v88, 0x1a000, v121
	s_cmp_eq_u32 s45, 0
	s_cbranch_scc1 .Lnerf_in_p0
	ds_read_b128 v[224:227], v88 offset:0
	ds_read_b128 v[228:231], v88 offset:1024
	ds_read_b128 v[232:235], v88 offset:2048
	ds_read_b128 v[236:239], v88 offset:3072
	ds_read_b128 v[240:243], v88 offset:4096
	ds_read_b128 v[244:247], v88 offset:5120
	ds_read_b128 v[248:251], v88 offset:6144
	ds_read_b128 v[252:255], v88 offset:7168
	s_waitcnt vmcnt(0)
	s_barrier
	s_branch .Lnerf_in_join
.Lnerf_in_p0:
	s_waitcnt vmcnt(0) lgkmcnt(0)
	s_barrier
	ds_read_b128 v[224:227], v88 offset:0
	ds_read_b128 v[228:231], v88 offset:1024
	ds_read_b128 v[232:235], v88 offset:2048
	ds_read_b128 v[236:239], v88 offset:3072
	ds_read_b128 v[240:243], v88 offset:4096
	ds_read_b128 v[244:247], v88 offset:5120
	ds_read_b128 v[248:251], v88 offset:6144
	ds_read_b128 v[252:255], v88 offset:7168
.Lnerf_in_join:
	s_waitcnt lgkmcnt(7)
	v_mfma_f32_16x16x32_bf16 v[64:67], v[224:227], v[208:211], 0
	v_mfma_f32_16x16x32_bf16 v[56:59], v[224:227], v[212:215], 0
	ds_read_b128 v[224:227], v88 offset:8192
	s_waitcnt lgkmcnt(7)
	v_mfma_f32_16x16x32_bf16 v[68:71], v[228:231], v[208:211], 0
	v_mfma_f32_16x16x32_bf16 v[60:63], v[228:231], v[212:215], 0
	ds_read_b128 v[228:231], v88 offset:9216
	s_waitcnt lgkmcnt(7)
	v_mfma_f32_16x16x32_bf16 v[64:67], v[232:235], v[216:219], v[64:67]
	v_mfma_f32_16x16x32_bf16 v[56:59], v[232:235], v[220:223], v[56:59]
	ds_read_b128 v[232:235], v88 offset:10240
	s_waitcnt lgkmcnt(7)
	v_mfma_f32_16x16x32_bf16 v[68:71], v[236:239], v[216:219], v[68:71]
	v_mfma_f32_16x16x32_bf16 v[60:63], v[236:239], v[220:223], v[60:63]
	ds_read_b128 v[236:239], v88 offset:11264
	s_waitcnt lgkmcnt(7)
	v_mfma_f32_16x16x32_bf16 v[80:83], v[240:243], v[208:211], 0
	v_cvt_pk_bf16_f32 v0, v64, v65
	v_cvt_pk_bf16_f32 v1, v66, v67
	v_mfma_f32_16x16x32_bf16 v[84:87], v[240:243], v[212:215], 0
	v_cvt_pk_bf16_f32 v4, v56, v57
	v_cvt_pk_bf16_f32 v5, v58, v59
	ds_read_b128 v[240:243], v88 offset:12288
	s_waitcnt lgkmcnt(7)
	v_mfma_f32_16x16x32_bf16 v[76:79], v[244:247], v[208:211], 0
	v_cvt_pk_bf16_f32 v2, v68, v69
	v_cvt_pk_bf16_f32 v3, v70, v71
	s_mov_b32 m0, s28
	s_mov_b32 s51, 0x8000
	v_mfma_f32_16x16x32_bf16 v[72:75], v[244:247], v[212:215], 0
	v_cvt_pk_bf16_f32 v6, v60, v61
	v_cvt_pk_bf16_f32 v7, v62, v63
	buffer_load_dwordx4 v125, s[36:39], s51 offen lds
	ds_read_b128 v[244:247], v88 offset:13312
	s_waitcnt lgkmcnt(7)
	v_mfma_f32_16x16x32_bf16 v[80:83], v[248:251], v[216:219], v[80:83]
	v_pk_max_i16 v0, v0, 0
	v_pk_max_i16 v1, v1, 0
	v_mfma_f32_16x16x32_bf16 v[84:87], v[248:251], v[220:223], v[84:87]
	v_pk_max_i16 v2, v2, 0
	v_pk_max_i16 v3, v3, 0
	ds_read_b128 v[248:251], v88 offset:14336
	s_waitcnt lgkmcnt(7)
	v_mfma_f32_16x16x32_bf16 v[76:79], v[252:255], v[216:219], v[76:79]
	v_pk_max_i16 v4, v4, 0
	v_pk_max_i16 v5, v5, 0
	v_mfma_f32_16x16x32_bf16 v[72:75], v[252:255], v[220:223], v[72:75]
	v_pk_max_i16 v6, v6, 0
	v_pk_max_i16 v7, v7, 0
	ds_read_b128 v[252:255], v88 offset:15360
	s_waitcnt lgkmcnt(7)
	v_mfma_f32_16x16x32_bf16 v[64:67], v[224:227], v[208:211], 0
	v_cvt_pk_bf16_f32 v12, v80, v81
	v_cvt_pk_bf16_f32 v13, v82, v83
	v_mfma_f32_16x16x32_bf16 v[56:59], v[224:227], v[212:215], 0
	v_cvt_pk_bf16_f32 v8, v84, v85
	v_cvt_pk_bf16_f32 v9, v86, v87
	ds_read_b128 v[224:227], v88 offset:16384
	s_waitcnt lgkmcnt(7)
	v_mfma_f32_16x16x32_bf16 v[68:71], v[228:231], v[208:211], 0
	v_cvt_pk_bf16_f32 v14, v76, v77
	v_cvt_pk_bf16_f32 v15, v78, v79
	s_mov_b32 m0, s29
	s_mov_b32 s51, 0xa000
	v_mfma_f32_16x16x32_bf16 v[60:63], v[228:231], v[212:215], 0
	v_cvt_pk_bf16_f32 v10, v72, v73
	v_cvt_pk_bf16_f32 v11, v74, v75
	buffer_load_dwordx4 v125, s[36:39], s51 offen lds
	ds_read_b128 v[228:231], v88 offset:17408
	s_waitcnt lgkmcnt(7)
	v_mfma_f32_16x16x32_bf16 v[64:67], v[232:235], v[216:219], v[64:67]
	v_pk_max_i16 v12, v12, 0
	v_pk_max_i16 v13, v13, 0
	v_mfma_f32_16x16x32_bf16 v[56:59], v[232:235], v[220:223], v[56:59]
	v_pk_max_i16 v14, v14, 0
	v_pk_max_i16 v15, v15, 0
	ds_read_b128 v[232:235], v88 offset:18432
	s_waitcnt lgkmcnt(7)
	v_mfma_f32_16x16x32_bf16 v[68:71], v[236:239], v[216:219], v[68:71]
	v_pk_max_i16 v8, v8, 0
	v_pk_max_i16 v9, v9, 0
	v_mfma_f32_16x16x32_bf16 v[60:63], v[236:239], v[220:223], v[60:63]
	v_pk_max_i16 v10, v10, 0
	v_pk_max_i16 v11, v11, 0
	ds_read_b128 v[236:239], v88 offset:19456
	s_waitcnt lgkmcnt(7)
	v_mfma_f32_16x16x32_bf16 v[80:83], v[240:243], v[208:211], 0
	v_cvt_pk_bf16_f32 v16, v64, v65
	v_cvt_pk_bf16_f32 v17, v66, v67
	v_mfma_f32_16x16x32_bf16 v[84:87], v[240:243], v[212:215], 0
	v_cvt_pk_bf16_f32 v20, v56, v57
	v_cvt_pk_bf16_f32 v21, v58, v59
	ds_read_b128 v[240:243], v88 offset:20480
	s_waitcnt lgkmcnt(7)
	v_mfma_f32_16x16x32_bf16 v[76:79], v[244:247], v[208:211], 0
	v_cvt_pk_bf16_f32 v18, v68, v69
	v_cvt_pk_bf16_f32 v19, v70, v71
	s_mov_b32 m0, s33
	s_mov_b32 s51, 0xc000
	v_mfma_f32_16x16x32_bf16 v[72:75], v[244:247], v[212:215], 0
	v_cvt_pk_bf16_f32 v22, v60, v61
	v_cvt_pk_bf16_f32 v23, v62, v63
	buffer_load_dwordx4 v125, s[36:39], s51 offen lds
	ds_read_b128 v[244:247], v88 offset:21504
	s_waitcnt lgkmcnt(7)
	v_mfma_f32_16x16x32_bf16 v[80:83], v[248:251], v[216:219], v[80:83]
	v_mfma_f32_16x16x32_bf16 v[84:87], v[248:251], v[220:223], v[84:87]
	ds_read_b128 v[248:251], v88 offset:22528
	s_waitcnt lgkmcnt(7)
	v_mfma_f32_16x16x32_bf16 v[76:79], v[252:255], v[216:219], v[76:79]
	v_mfma_f32_16x16x32_bf16 v[72:75], v[252:255], v[220:223], v[72:75]
	ds_read_b128 v[252:255], v88 offset:23552
	s_waitcnt lgkmcnt(7)
	v_mfma_f32_16x16x32_bf16 v[64:67], v[224:227], v[208:211], 0
	v_cvt_pk_bf16_f32 v24, v80, v81
	v_cvt_pk_bf16_f32 v25, v82, v83
	v_mfma_f32_16x16x32_bf16 v[56:59], v[224:227], v[212:215], 0
	v_cvt_pk_bf16_f32 v28, v84, v85
	v_cvt_pk_bf16_f32 v29, v86, v87
	ds_read_b128 v[224:227], v88 offset:24576
	s_waitcnt lgkmcnt(7)
	v_mfma_f32_16x16x32_bf16 v[68:71], v[228:231], v[208:211], 0
	v_cvt_pk_bf16_f32 v26, v76, v77
	v_cvt_pk_bf16_f32 v27, v78, v79
	s_mov_b32 m0, s34
	s_mov_b32 s51, 0xe000
	v_mfma_f32_16x16x32_bf16 v[60:63], v[228:231], v[212:215], 0
	v_cvt_pk_bf16_f32 v30, v72, v73
	v_cvt_pk_bf16_f32 v31, v74, v75
	buffer_load_dwordx4 v125, s[36:39], s51 offen lds
	ds_read_b128 v[228:231], v88 offset:25600
	s_waitcnt lgkmcnt(7)
	v_mfma_f32_16x16x32_bf16 v[64:67], v[232:235], v[216:219], v[64:67]
	v_mfma_f32_16x16x32_bf16 v[56:59], v[232:235], v[220:223], v[56:59]
	ds_read_b128 v[232:235], v88 offset:26624
	s_waitcnt lgkmcnt(7)
	v_mfma_f32_16x16x32_bf16 v[68:71], v[236:239], v[216:219], v[68:71]
	v_mfma_f32_16x16x32_bf16 v[60:63], v[236:239], v[220:223], v[60:63]
	ds_read_b128 v[236:239], v88 offset:27648
	s_waitcnt lgkmcnt(7)
	v_mfma_f32_16x16x32_bf16 v[80:83], v[240:243], v[208:211], 0
	v_cvt_pk_bf16_f32 v32, v64, v65
	v_cvt_pk_bf16_f32 v33, v66, v67
	v_mfma_f32_16x16x32_bf16 v[84:87], v[240:243], v[212:215], 0
	v_cvt_pk_bf16_f32 v36, v56, v57
	v_cvt_pk_bf16_f32 v37, v58, v59
	ds_read_b128 v[240:243], v88 offset:28672
	s_waitcnt lgkmcnt(7)
	v_mfma_f32_16x16x32_bf16 v[76:79], v[244:247], v[208:211], 0
	v_cvt_pk_bf16_f32 v34, v68, v69
	v_cvt_pk_bf16_f32 v35, v70, v71
	v_mfma_f32_16x16x32_bf16 v[72:75], v[244:247], v[212:215], 0
	v_cvt_pk_bf16_f32 v38, v60, v61
	v_cvt_pk_bf16_f32 v39, v62, v63
	ds_read_b128 v[244:247], v88 offset:29696
	s_waitcnt lgkmcnt(7)
	v_mfma_f32_16x16x32_bf16 v[80:83], v[248:251], v[216:219], v[80:83]
	v_mfma_f32_16x16x32_bf16 v[84:87], v[248:251], v[220:223], v[84:87]
	ds_read_b128 v[248:251], v88 offset:30720
	s_waitcnt lgkmcnt(7)
	v_mfma_f32_16x16x32_bf16 v[76:79], v[252:255], v[216:219], v[76:79]
	v_mfma_f32_16x16x32_bf16 v[72:75], v[252:255], v[220:223], v[72:75]
	ds_read_b128 v[252:255], v88 offset:31744
	s_waitcnt lgkmcnt(7)
	v_mfma_f32_16x16x32_bf16 v[64:67], v[224:227], v[208:211], 0
	v_cvt_pk_bf16_f32 v40, v80, v81
	v_cvt_pk_bf16_f32 v41, v82, v83
	v_mfma_f32_16x16x32_bf16 v[56:59], v[224:227], v[212:215], 0
	v_cvt_pk_bf16_f32 v44, v84, v85
	v_cvt_pk_bf16_f32 v45, v86, v87
	s_waitcnt lgkmcnt(6)
	v_mfma_f32_16x16x32_bf16 v[68:71], v[228:231], v[208:211], 0
	v_cvt_pk_bf16_f32 v42, v76, v77
	v_cvt_pk_bf16_f32 v43, v78, v79
	v_mfma_f32_16x16x32_bf16 v[60:63], v[228:231], v[212:215], 0
	v_cvt_pk_bf16_f32 v46, v72, v73
	v_cvt_pk_bf16_f32 v47, v74, v75
	s_waitcnt lgkmcnt(5)
	v_mfma_f32_16x16x32_bf16 v[64:67], v[232:235], v[216:219], v[64:67]
	v_mfma_f32_16x16x32_bf16 v[56:59], v[232:235], v[220:223], v[56:59]
	s_waitcnt lgkmcnt(4)
	v_mfma_f32_16x16x32_bf16 v[68:71], v[236:239], v[216:219], v[68:71]
	v_mfma_f32_16x16x32_bf16 v[60:63], v[236:239], v[220:223], v[60:63]
	s_cmp_lt_u32 s31, 2
	s_cbranch_scc0 .Lnerf_hid_b_first
	s_waitcnt vmcnt(0) lgkmcnt(0)
	s_barrier
	ds_read_b128 v[224:227], v121 offset:40960
	ds_read_b128 v[228:231], v121 offset:41984
	ds_read_b128 v[152:155], v183 offset:0
	ds_read_b128 v[156:159], v183 offset:64
	v_mfma_f32_16x16x32_bf16 v[80:83], v[240:243], v[208:211], 0
	ds_read_b128 v[232:235], v121 offset:43008
	v_cvt_pk_bf16_f32 v48, v64, v65
	v_cvt_pk_bf16_f32 v49, v66, v67
	v_mfma_f32_16x16x32_bf16 v[84:87], v[240:243], v[212:215], 0
	ds_read_b128 v[236:239], v121 offset:44032
	v_cvt_pk_bf16_f32 v52, v56, v57
	v_cvt_pk_bf16_f32 v53, v58, v59
	ds_read_b128 v[240:243], v121 offset:45056
	v_mfma_f32_16x16x32_bf16 v[76:79], v[244:247], v[208:211], 0
	v_cvt_pk_bf16_f32 v50, v68, v69
	v_cvt_pk_bf16_f32 v51, v70, v71
	v_mfma_f32_16x16x32_bf16 v[72:75], v[244:247], v[212:215], 0
	v_cvt_pk_bf16_f32 v54, v60, v61
	v_cvt_pk_bf16_f32 v55, v62, v63
	ds_read_b128 v[244:247], v121 offset:46080
	v_mfma_f32_16x16x32_bf16 v[80:83], v[248:251], v[216:219], v[80:83]
	v_pk_max_i16 v48, v48, 0
	v_pk_max_i16 v49, v49, 0
	v_mfma_f32_16x16x32_bf16 v[84:87], v[248:251], v[220:223], v[84:87]
	v_pk_max_i16 v50, v50, 0
	v_pk_max_i16 v51, v51, 0
	ds_read_b128 v[248:251], v121 offset:47104
	v_mfma_f32_16x16x32_bf16 v[76:79], v[252:255], v[216:219], v[76:79]
	v_pk_max_i16 v52, v52, 0
	v_pk_max_i16 v53, v53, 0
	v_mfma_f32_16x16x32_bf16 v[72:75], v[252:255], v[220:223], v[72:75]
	v_pk_max_i16 v54, v54, 0
	v_pk_max_i16 v55, v55, 0
	ds_read_b128 v[252:255], v121 offset:48128
	s_setprio 3
	s_waitcnt lgkmcnt(6)
	v_mfma_f32_16x16x32_bf16 v[64:67], v[224:227], v[0:3], v[152:155]
	v_pk_max_i16 v16, v16, 0
	v_pk_max_i16 v17, v17, 0
	v_mfma_f32_16x16x32_bf16 v[68:71], v[228:231], v[0:3], v[156:159]
	v_pk_max_i16 v18, v18, 0
	v_pk_max_i16 v19, v19, 0
	v_mfma_f32_16x16x32_bf16 v[60:63], v[228:231], v[4:7], v[156:159]
	v_pk_max_i16 v20, v20, 0
	v_pk_max_i16 v21, v21, 0
	v_mfma_f32_16x16x32_bf16 v[56:59], v[224:227], v[4:7], v[152:155]
	v_pk_max_i16 v22, v22, 0
	v_pk_max_i16 v23, v23, 0
	ds_read_b128 v[224:227], v121 offset:49152
	ds_read_b128 v[228:231], v121 offset:50176
	s_waitcnt lgkmcnt(6)
	ds_read_b128 v[160:163], v183 offset:128
	ds_read_b128 v[164:167], v183 offset:192
	v_mfma_f32_16x16x32_bf16 v[64:67], v[232:235], v[12:15], v[64:67]
	v_pk_max_i16 v24, v24, 0
	v_pk_max_i16 v25, v25, 0
	v_cvt_pk_bf16_f32 v112, v80, v81
	v_mfma_f32_16x16x32_bf16 v[68:71], v[236:239], v[12:15], v[68:71]
	v_pk_max_i16 v26, v26, 0
	v_pk_max_i16 v27, v27, 0
	s_mov_b32 m0, s35
	s_add_i32 s51, s50, 0x0
	v_cvt_pk_bf16_f32 v113, v82, v83
	v_mfma_f32_16x16x32_bf16 v[60:63], v[236:239], v[8:11], v[60:63]
	v_pk_max_i16 v28, v28, 0
	v_pk_max_i16 v29, v29, 0
	buffer_load_dwordx4 v125, s[36:39], s51 offen lds
	v_cvt_pk_bf16_f32 v114, v76, v77
	v_mfma_f32_16x16x32_bf16 v[56:59], v[232:235], v[8:11], v[56:59]
	v_pk_max_i16 v30, v30, 0
	v_pk_max_i16 v31, v31, 0
	v_cvt_pk_bf16_f32 v115, v78, v79
	ds_read_b128 v[232:235], v121 offset:51200
	ds_read_b128 v[236:239], v121 offset:52224
	s_waitcnt lgkmcnt(8)
	v_mfma_f32_16x16x32_bf16 v[64:67], v[240:243], v[16:19], v[64:67]
	v_pk_max_i16 v32, v32, 0
	v_pk_max_i16 v33, v33, 0
	v_cvt_pk_bf16_f32 v116, v84, v85
	v_mfma_f32_16x16x32_bf16 v[68:71], v[244:247], v[16:19], v[68:71]
	v_pk_max_i16 v34, v34, 0
	v_pk_max_i16 v35, v35, 0
	s_mov_b32 m0, s42
	s_add_i32 s51, s50, 0x2000
	v_cvt_pk_bf16_f32 v117, v86, v87
	v_mfma_f32_16x16x32_bf16 v[60:63], v[244:247], v[20:23], v[60:63]
	v_pk_max_i16 v36, v36, 0
	v_pk_max_i16 v37, v37, 0
	buffer_load_dwordx4 v125, s[36:39], s51 offen lds
	v_cvt_pk_bf16_f32 v118, v72, v73
	v_mfma_f32_16x16x32_bf16 v[56:59], v[240:243], v[20:23], v[56:59]
	v_pk_max_i16 v38, v38, 0
	v_pk_max_i16 v39, v39, 0
	v_cvt_pk_bf16_f32 v119, v74, v75
	ds_read_b128 v[240:243], v121 offset:53248
	ds_read_b128 v[244:247], v121 offset:54272
	s_waitcnt lgkmcnt(8)
	v_mfma_f32_16x16x32_bf16 v[64:67], v[248:251], v[24:27], v[64:67]
	v_pk_max_i16 v40, v40, 0
	v_pk_max_i16 v41, v41, 0
	v_pk_max_i16 v112, v112, 0
	v_mfma_f32_16x16x32_bf16 v[68:71], v[252:255], v[24:27], v[68:71]
	v_pk_max_i16 v42, v42, 0
	v_pk_max_i16 v43, v43, 0
	s_mov_b32 m0, s41
	s_add_i32 s51, s50, 0x4000
	v_pk_max_i16 v113, v113, 0
	v_mfma_f32_16x16x32_bf16 v[60:63], v[252:255], v[28:31], v[60:63]
	v_pk_max_i16 v44, v44, 0
	v_pk_max_i16 v45, v45, 0
	buffer_load_dwordx4 v125, s[36:39], s51 offen lds
	v_pk_max_i16 v114, v114, 0
	v_mfma_f32_16x16x32_bf16 v[56:59], v[248:251], v[28:31], v[56:59]
	v_pk_max_i16 v46, v46, 0
	v_pk_max_i16 v47, v47, 0
	v_pk_max_i16 v115, v115, 0
	ds_read_b128 v[248:251], v121 offset:55296
	ds_read_b128 v[252:255], v121 offset:56320
	s_setprio 2
	s_waitcnt lgkmcnt(8)
	v_mfma_f32_16x16x32_bf16 v[64:67], v[224:227], v[32:35], v[64:67]
	v_pk_max_i16 v116, v116, 0
	v_mfma_f32_16x16x32_bf16 v[68:71], v[228:231], v[32:35], v[68:71]
	s_mov_b32 m0, s40
	s_add_i32 s51, s50, 0x6000
	v_pk_max_i16 v117, v117, 0
	v_mfma_f32_16x16x32_bf16 v[60:63], v[228:231], v[36:39], v[60:63]
	buffer_load_dwordx4 v125, s[36:39], s51 offen lds
	v_pk_max_i16 v118, v118, 0
	v_mfma_f32_16x16x32_bf16 v[56:59], v[224:227], v[36:39], v[56:59]
	v_pk_max_i16 v119, v119, 0
	ds_read_b128 v[224:227], v121 offset:57344
	ds_read_b128 v[228:231], v121 offset:58368
	s_waitcnt lgkmcnt(6)
	v_mfma_f32_16x16x32_bf16 v[64:67], v[232:235], v[40:43], v[64:67]
	v_mfma_f32_16x16x32_bf16 v[68:71], v[236:239], v[40:43], v[68:71]
	v_mfma_f32_16x16x32_bf16 v[60:63], v[236:239], v[44:47], v[60:63]
	v_mfma_f32_16x16x32_bf16 v[56:59], v[232:235], v[44:47], v[56:59]
	ds_read_b128 v[232:235], v121 offset:59392
	ds_read_b128 v[236:239], v121 offset:60416
	s_waitcnt lgkmcnt(6)
	ds_read_b128 v[152:155], v183 offset:256
	ds_read_b128 v[156:159], v183 offset:320
	v_mfma_f32_16x16x32_bf16 v[64:67], v[240:243], v[48:51], v[64:67]
	v_mfma_f32_16x16x32_bf16 v[68:71], v[244:247], v[48:51], v[68:71]
	v_mfma_f32_16x16x32_bf16 v[60:63], v[244:247], v[52:55], v[60:63]
	v_mfma_f32_16x16x32_bf16 v[56:59], v[240:243], v[52:55], v[56:59]
	ds_read_b128 v[240:243], v121 offset:61440
	ds_read_b128 v[244:247], v121 offset:62464
	s_waitcnt lgkmcnt(8)
	v_mfma_f32_16x16x32_bf16 v[64:67], v[248:251], v[112:115], v[64:67]
	v_mfma_f32_16x16x32_bf16 v[68:71], v[252:255], v[112:115], v[68:71]
	v_mfma_f32_16x16x32_bf16 v[60:63], v[252:255], v[116:119], v[60:63]
	v_mfma_f32_16x16x32_bf16 v[56:59], v[248:251], v[116:119], v[56:59]
	ds_read_b128 v[248:251], v121 offset:63488
	ds_read_b128 v[252:255], v121 offset:64512
	s_setprio 1
	s_waitcnt lgkmcnt(8)
	v_mfma_f32_16x16x32_bf16 v[80:83], v[224:227], v[0:3], v[160:163]
	v_mfma_f32_16x16x32_bf16 v[76:79], v[228:231], v[0:3], v[164:167]
	v_mfma_f32_16x16x32_bf16 v[72:75], v[228:231], v[4:7], v[164:167]
	v_mfma_f32_16x16x32_bf16 v[84:87], v[224:227], v[4:7], v[160:163]
	ds_read_b128 v[224:227], v126 offset:57344
	ds_read_b128 v[228:231], v126 offset:58368
	s_waitcnt lgkmcnt(8)
	v_mfma_f32_16x16x32_bf16 v[80:83], v[232:235], v[12:15], v[80:83]
	v_cvt_pk_bf16_f32 v88, v64, v65
	v_mfma_f32_16x16x32_bf16 v[76:79], v[236:239], v[12:15], v[76:79]
	v_cvt_pk_bf16_f32 v89, v66, v67
	v_mfma_f32_16x16x32_bf16 v[72:75], v[236:239], v[8:11], v[72:75]
	v_cvt_pk_bf16_f32 v90, v68, v69
	v_mfma_f32_16x16x32_bf16 v[84:87], v[232:235], v[8:11], v[84:87]
	v_cvt_pk_bf16_f32 v91, v70, v71
	ds_read_b128 v[232:235], v126 offset:59392
	ds_read_b128 v[236:239], v126 offset:60416
	s_waitcnt lgkmcnt(6)
	v_mfma_f32_16x16x32_bf16 v[80:83], v[240:243], v[16:19], v[80:83]
	v_cvt_pk_bf16_f32 v92, v56, v57
	v_mfma_f32_16x16x32_bf16 v[76:79], v[244:247], v[16:19], v[76:79]
	v_cvt_pk_bf16_f32 v93, v58, v59
	v_mfma_f32_16x16x32_bf16 v[72:75], v[244:247], v[20:23], v[72:75]
	v_cvt_pk_bf16_f32 v94, v60, v61
	v_mfma_f32_16x16x32_bf16 v[84:87], v[240:243], v[20:23], v[84:87]
	v_cvt_pk_bf16_f32 v95, v62, v63
	ds_read_b128 v[240:243], v126 offset:61440
	ds_read_b128 v[244:247], v126 offset:62464
	s_waitcnt lgkmcnt(6)
	v_mfma_f32_16x16x32_bf16 v[80:83], v[248:251], v[24:27], v[80:83]
	v_pk_max_i16 v88, v88, 0
	v_mfma_f32_16x16x32_bf16 v[76:79], v[252:255], v[24:27], v[76:79]
	v_pk_max_i16 v89, v89, 0
	v_mfma_f32_16x16x32_bf16 v[72:75], v[252:255], v[28:31], v[72:75]
	v_pk_max_i16 v90, v90, 0
	v_mfma_f32_16x16x32_bf16 v[84:87], v[248:251], v[28:31], v[84:87]
	v_pk_max_i16 v91, v91, 0
	ds_read_b128 v[248:251], v126 offset:63488
	ds_read_b128 v[252:255], v126 offset:64512
	s_setprio 0
	s_waitcnt lgkmcnt(6)
	v_mfma_f32_16x16x32_bf16 v[80:83], v[224:227], v[32:35], v[80:83]
	v_pk_max_i16 v92, v92, 0
	v_mfma_f32_16x16x32_bf16 v[76:79], v[228:231], v[32:35], v[76:79]
	v_pk_max_i16 v93, v93, 0
	v_mfma_f32_16x16x32_bf16 v[72:75], v[228:231], v[36:39], v[72:75]
	v_pk_max_i16 v94, v94, 0
	v_mfma_f32_16x16x32_bf16 v[84:87], v[224:227], v[36:39], v[84:87]
	v_pk_max_i16 v95, v95, 0
	s_waitcnt lgkmcnt(4)
	v_mfma_f32_16x16x32_bf16 v[80:83], v[232:235], v[40:43], v[80:83]
	v_mfma_f32_16x16x32_bf16 v[76:79], v[236:239], v[40:43], v[76:79]
	v_mfma_f32_16x16x32_bf16 v[72:75], v[236:239], v[44:47], v[72:75]
	v_mfma_f32_16x16x32_bf16 v[84:87], v[232:235], v[44:47], v[84:87]
	s_branch .Lnerf_hid_a1

.Lnerf_hid_b_first:
	s_waitcnt vmcnt(0) lgkmcnt(0)
	s_barrier
	ds_read_b128 v[224:227], v121 offset:40960
	ds_read_b128 v[228:231], v121 offset:41984
	ds_read_b128 v[152:155], v183 offset:0
	ds_read_b128 v[156:159], v183 offset:64
	v_mfma_f32_16x16x32_bf16 v[80:83], v[240:243], v[208:211], 0
	ds_read_b128 v[232:235], v121 offset:43008
	v_cvt_pk_bf16_f32 v48, v64, v65
	v_cvt_pk_bf16_f32 v49, v66, v67
	v_mfma_f32_16x16x32_bf16 v[84:87], v[240:243], v[212:215], 0
	ds_read_b128 v[236:239], v121 offset:44032
	v_cvt_pk_bf16_f32 v52, v56, v57
	v_cvt_pk_bf16_f32 v53, v58, v59
	ds_read_b128 v[240:243], v121 offset:45056
	v_mfma_f32_16x16x32_bf16 v[76:79], v[244:247], v[208:211], 0
	v_cvt_pk_bf16_f32 v50, v68, v69
	v_cvt_pk_bf16_f32 v51, v70, v71
	v_mfma_f32_16x16x32_bf16 v[72:75], v[244:247], v[212:215], 0
	v_cvt_pk_bf16_f32 v54, v60, v61
	v_cvt_pk_bf16_f32 v55, v62, v63
	ds_read_b128 v[244:247], v121 offset:46080
	v_mfma_f32_16x16x32_bf16 v[80:83], v[248:251], v[216:219], v[80:83]
	v_pk_max_i16 v48, v48, 0
	v_pk_max_i16 v49, v49, 0
	v_mfma_f32_16x16x32_bf16 v[84:87], v[248:251], v[220:223], v[84:87]
	v_pk_max_i16 v50, v50, 0
	v_pk_max_i16 v51, v51, 0
	ds_read_b128 v[248:251], v121 offset:47104
	v_mfma_f32_16x16x32_bf16 v[76:79], v[252:255], v[216:219], v[76:79]
	v_pk_max_i16 v52, v52, 0
	v_pk_max_i16 v53, v53, 0
	v_mfma_f32_16x16x32_bf16 v[72:75], v[252:255], v[220:223], v[72:75]
	v_pk_max_i16 v54, v54, 0
	v_pk_max_i16 v55, v55, 0
	ds_read_b128 v[252:255], v121 offset:48128
	s_setprio 3
	s_waitcnt lgkmcnt(6)
	v_mfma_f32_16x16x32_bf16 v[64:67], v[224:227], v[0:3], v[152:155]
	v_pk_max_i16 v16, v16, 0
	v_pk_max_i16 v17, v17, 0
	v_mfma_f32_16x16x32_bf16 v[68:71], v[228:231], v[0:3], v[156:159]
	v_pk_max_i16 v18, v18, 0
	v_pk_max_i16 v19, v19, 0
	v_mfma_f32_16x16x32_bf16 v[60:63], v[228:231], v[4:7], v[156:159]
	v_pk_max_i16 v20, v20, 0
	v_pk_max_i16 v21, v21, 0
	v_mfma_f32_16x16x32_bf16 v[56:59], v[224:227], v[4:7], v[152:155]
	v_pk_max_i16 v22, v22, 0
	v_pk_max_i16 v23, v23, 0
	ds_read_b128 v[224:227], v121 offset:49152
	ds_read_b128 v[228:231], v121 offset:50176
	s_waitcnt lgkmcnt(6)
	ds_read_b128 v[160:163], v183 offset:128
	ds_read_b128 v[164:167], v183 offset:192
	v_mfma_f32_16x16x32_bf16 v[64:67], v[232:235], v[12:15], v[64:67]
	v_pk_max_i16 v24, v24, 0
	v_pk_max_i16 v25, v25, 0
	v_cvt_pk_bf16_f32 v112, v80, v81
	v_mfma_f32_16x16x32_bf16 v[68:71], v[236:239], v[12:15], v[68:71]
	v_pk_max_i16 v26, v26, 0
	v_pk_max_i16 v27, v27, 0
	v_cvt_pk_bf16_f32 v113, v82, v83
	v_mfma_f32_16x16x32_bf16 v[60:63], v[236:239], v[8:11], v[60:63]
	v_pk_max_i16 v28, v28, 0
	v_pk_max_i16 v29, v29, 0
	v_cvt_pk_bf16_f32 v114, v76, v77
	v_mfma_f32_16x16x32_bf16 v[56:59], v[232:235], v[8:11], v[56:59]
	v_pk_max_i16 v30, v30, 0
	v_pk_max_i16 v31, v31, 0
	v_cvt_pk_bf16_f32 v115, v78, v79
	ds_read_b128 v[232:235], v121 offset:51200
	ds_read_b128 v[236:239], v121 offset:52224
	s_waitcnt lgkmcnt(8)
	v_mfma_f32_16x16x32_bf16 v[64:67], v[240:243], v[16:19], v[64:67]
	v_pk_max_i16 v32, v32, 0
	v_pk_max_i16 v33, v33, 0
	v_cvt_pk_bf16_f32 v116, v84, v85
	v_mfma_f32_16x16x32_bf16 v[68:71], v[244:247], v[16:19], v[68:71]
	v_pk_max_i16 v34, v34, 0
	v_pk_max_i16 v35, v35, 0
	v_cvt_pk_bf16_f32 v117, v86, v87
	v_mfma_f32_16x16x32_bf16 v[60:63], v[244:247], v[20:23], v[60:63]
	v_pk_max_i16 v36, v36, 0
	v_pk_max_i16 v37, v37, 0
	v_cvt_pk_bf16_f32 v118, v72, v73
	v_mfma_f32_16x16x32_bf16 v[56:59], v[240:243], v[20:23], v[56:59]
	v_pk_max_i16 v38, v38, 0
	v_pk_max_i16 v39, v39, 0
	v_cvt_pk_bf16_f32 v119, v74, v75
	ds_read_b128 v[240:243], v121 offset:53248
	ds_read_b128 v[244:247], v121 offset:54272
	s_waitcnt lgkmcnt(8)
	v_mfma_f32_16x16x32_bf16 v[64:67], v[248:251], v[24:27], v[64:67]
	v_pk_max_i16 v40, v40, 0
	v_pk_max_i16 v41, v41, 0
	v_pk_max_i16 v112, v112, 0
	v_mfma_f32_16x16x32_bf16 v[68:71], v[252:255], v[24:27], v[68:71]
	v_pk_max_i16 v42, v42, 0
	v_pk_max_i16 v43, v43, 0
	v_pk_max_i16 v113, v113, 0
	v_mfma_f32_16x16x32_bf16 v[60:63], v[252:255], v[28:31], v[60:63]
	v_pk_max_i16 v44, v44, 0
	v_pk_max_i16 v45, v45, 0
	v_pk_max_i16 v114, v114, 0
	v_mfma_f32_16x16x32_bf16 v[56:59], v[248:251], v[28:31], v[56:59]
	v_pk_max_i16 v46, v46, 0
	v_pk_max_i16 v47, v47, 0
	v_pk_max_i16 v115, v115, 0
	ds_read_b128 v[248:251], v121 offset:55296
	ds_read_b128 v[252:255], v121 offset:56320
	s_setprio 2
	s_waitcnt lgkmcnt(8)
	v_mfma_f32_16x16x32_bf16 v[64:67], v[224:227], v[32:35], v[64:67]
	v_pk_max_i16 v116, v116, 0
	v_mfma_f32_16x16x32_bf16 v[68:71], v[228:231], v[32:35], v[68:71]
	v_pk_max_i16 v117, v117, 0
	v_mfma_f32_16x16x32_bf16 v[60:63], v[228:231], v[36:39], v[60:63]
	v_pk_max_i16 v118, v118, 0
	v_mfma_f32_16x16x32_bf16 v[56:59], v[224:227], v[36:39], v[56:59]
	v_pk_max_i16 v119, v119, 0
	ds_read_b128 v[224:227], v121 offset:57344
	ds_read_b128 v[228:231], v121 offset:58368
	s_waitcnt lgkmcnt(6)
	v_mfma_f32_16x16x32_bf16 v[64:67], v[232:235], v[40:43], v[64:67]
	v_mfma_f32_16x16x32_bf16 v[68:71], v[236:239], v[40:43], v[68:71]
	s_mov_b32 m0, s35
	s_add_i32 s51, s50, 0x0
	v_mfma_f32_16x16x32_bf16 v[60:63], v[236:239], v[44:47], v[60:63]
	buffer_load_dwordx4 v125, s[36:39], s51 offen lds
	v_mfma_f32_16x16x32_bf16 v[56:59], v[232:235], v[44:47], v[56:59]
	ds_read_b128 v[232:235], v121 offset:59392
	ds_read_b128 v[236:239], v121 offset:60416
	s_waitcnt lgkmcnt(6)
	ds_read_b128 v[152:155], v183 offset:256
	ds_read_b128 v[156:159], v183 offset:320
	v_mfma_f32_16x16x32_bf16 v[64:67], v[240:243], v[48:51], v[64:67]
	v_mfma_f32_16x16x32_bf16 v[68:71], v[244:247], v[48:51], v[68:71]
	s_mov_b32 m0, s42
	s_add_i32 s51, s50, 0x2000
	v_mfma_f32_16x16x32_bf16 v[60:63], v[244:247], v[52:55], v[60:63]
	buffer_load_dwordx4 v125, s[36:39], s51 offen lds
	v_mfma_f32_16x16x32_bf16 v[56:59], v[240:243], v[52:55], v[56:59]
	ds_read_b128 v[240:243], v121 offset:61440
	ds_read_b128 v[244:247], v121 offset:62464
	s_waitcnt lgkmcnt(8)
	v_mfma_f32_16x16x32_bf16 v[64:67], v[248:251], v[112:115], v[64:67]
	v_mfma_f32_16x16x32_bf16 v[68:71], v[252:255], v[112:115], v[68:71]
	s_mov_b32 m0, s41
	s_add_i32 s51, s50, 0x4000
	v_mfma_f32_16x16x32_bf16 v[60:63], v[252:255], v[116:119], v[60:63]
	buffer_load_dwordx4 v125, s[36:39], s51 offen lds
	v_mfma_f32_16x16x32_bf16 v[56:59], v[248:251], v[116:119], v[56:59]
	ds_read_b128 v[248:251], v121 offset:63488
	ds_read_b128 v[252:255], v121 offset:64512
	s_setprio 1
	s_waitcnt lgkmcnt(8)
	v_mfma_f32_16x16x32_bf16 v[80:83], v[224:227], v[0:3], v[160:163]
	v_mfma_f32_16x16x32_bf16 v[76:79], v[228:231], v[0:3], v[164:167]
	s_mov_b32 m0, s40
	s_add_i32 s51, s50, 0x6000
	v_mfma_f32_16x16x32_bf16 v[72:75], v[228:231], v[4:7], v[164:167]
	buffer_load_dwordx4 v125, s[36:39], s51 offen lds
	v_mfma_f32_16x16x32_bf16 v[84:87], v[224:227], v[4:7], v[160:163]
	ds_read_b128 v[224:227], v126 offset:57344
	ds_read_b128 v[228:231], v126 offset:58368
	s_waitcnt lgkmcnt(8)
	v_mfma_f32_16x16x32_bf16 v[80:83], v[232:235], v[12:15], v[80:83]
	v_cvt_pk_bf16_f32 v88, v64, v65
	v_mfma_f32_16x16x32_bf16 v[76:79], v[236:239], v[12:15], v[76:79]
	v_cvt_pk_bf16_f32 v89, v66, v67
	v_mfma_f32_16x16x32_bf16 v[72:75], v[236:239], v[8:11], v[72:75]
	v_cvt_pk_bf16_f32 v90, v68, v69
	v_mfma_f32_16x16x32_bf16 v[84:87], v[232:235], v[8:11], v[84:87]
	v_cvt_pk_bf16_f32 v91, v70, v71
	ds_read_b128 v[232:235], v126 offset:59392
	ds_read_b128 v[236:239], v126 offset:60416
	s_waitcnt lgkmcnt(6)
	v_mfma_f32_16x16x32_bf16 v[80:83], v[240:243], v[16:19], v[80:83]
	v_cvt_pk_bf16_f32 v92, v56, v57
	v_mfma_f32_16x16x32_bf16 v[76:79], v[244:247], v[16:19], v[76:79]
	v_cvt_pk_bf16_f32 v93, v58, v59
	v_mfma_f32_16x16x32_bf16 v[72:75], v[244:247], v[20:23], v[72:75]
	v_cvt_pk_bf16_f32 v94, v60, v61
	v_mfma_f32_16x16x32_bf16 v[84:87], v[240:243], v[20:23], v[84:87]
	v_cvt_pk_bf16_f32 v95, v62, v63
	ds_read_b128 v[240:243], v126 offset:61440
	ds_read_b128 v[244:247], v126 offset:62464
	s_waitcnt lgkmcnt(6)
	v_mfma_f32_16x16x32_bf16 v[80:83], v[248:251], v[24:27], v[80:83]
	v_pk_max_i16 v88, v88, 0
	v_mfma_f32_16x16x32_bf16 v[76:79], v[252:255], v[24:27], v[76:79]
	v_pk_max_i16 v89, v89, 0
	v_mfma_f32_16x16x32_bf16 v[72:75], v[252:255], v[28:31], v[72:75]
	v_pk_max_i16 v90, v90, 0
	v_mfma_f32_16x16x32_bf16 v[84:87], v[248:251], v[28:31], v[84:87]
	v_pk_max_i16 v91, v91, 0
	ds_read_b128 v[248:251], v126 offset:63488
	ds_read_b128 v[252:255], v126 offset:64512
	s_setprio 0
	s_waitcnt lgkmcnt(6)
	v_mfma_f32_16x16x32_bf16 v[80:83], v[224:227], v[32:35], v[80:83]
	v_pk_max_i16 v92, v92, 0
	v_mfma_f32_16x16x32_bf16 v[76:79], v[228:231], v[32:35], v[76:79]
	v_pk_max_i16 v93, v93, 0
	v_mfma_f32_16x16x32_bf16 v[72:75], v[228:231], v[36:39], v[72:75]
	v_pk_max_i16 v94, v94, 0
	v_mfma_f32_16x16x32_bf16 v[84:87], v[224:227], v[36:39], v[84:87]
	v_pk_max_i16 v95, v95, 0
	s_waitcnt lgkmcnt(4)
	v_mfma_f32_16x16x32_bf16 v[80:83], v[232:235], v[40:43], v[80:83]
	v_mfma_f32_16x16x32_bf16 v[76:79], v[236:239], v[40:43], v[76:79]
	v_mfma_f32_16x16x32_bf16 v[72:75], v[236:239], v[44:47], v[72:75]
	v_mfma_f32_16x16x32_bf16 v[84:87], v[232:235], v[44:47], v[84:87]
	s_branch .Lnerf_hid_b1
